# fp8 conversion items re-dealt so the 16 workgroups converting at the same time read whole rows of the f32 expert weights (128 consecutive items per step), on top of nt loads + reversed P6
# baseline (speedup 1.0000x reference)
; #define LAS __attribute__((address_space(3)))
; __device__ __forceinline__ int fresh_lane() { unsigned z = 0u; asm volatile("" : "+v"(z)); return (int)__builtin_amdgcn_mbcnt_hi(~0u, __builtin_amdgcn_mbcnt_lo(~0u, z)); }
; __device__ __forceinline__ F8Item f8_item(const P& p, int r) {
;     constexpr int I_W1 = 8 * 64, I_W2 = 8 * 32; F8Item it;
;     if (r < NE * I_W1) { const int e = r / I_W1, q = r % I_W1; it.W = p.w1 + (size_t)e * DM * 2048; it.WT = p.ws + WS_W1T + (size_t)e * 2048 * DM; it.N = 2048; it.k0 = 128 * (q / 64); it.n0 = 32 * (q % 64); it.map = 1; }
;     else { r -= NE * I_W1; const int e = r / I_W2, q = r % I_W2; it.W = p.w2 + (size_t)e * DM * DM; it.WT = p.ws + WS_W2T + (size_t)e * DM * DM; it.N = DM; it.k0 = 128 * (q / 32); it.n0 = 32 * (q % 32); it.map = 0; }
;     return it;
; }
; __device__ __forceinline__ void f8_share(const P& p, LAS unsigned char* ring, int G, int vcu, int wave) {
;     const int lane = fresh_lane(); LAS float* scr = (LAS float*)(ring + wave * 16384);
;     const int gw = vcu * NWAVES + wave, NGW = G * NWAVES; constexpr int NF8 = NE * (8 * 64 + 8 * 32);
;     f32x4 va[16], vb[16]; int it = gw;
;     F8Item ia = f8_item(p, it < NF8 ? it : 0), ib = ia;
;     if (it < NF8) f8_load(ia, va, lane);
;     if (it + NGW < NF8) { ib = f8_item(p, it + NGW); f8_load(ib, vb, lane); }
.LBB7_394:
	s_and_b32 s78, s95, 15
	s_add_u32 s79, s30, 0x3c0000
	s_addc_u32 s80, s31, 0
	s_add_u32 s0, s30, 0x37000000
	v_writelane_b32 v254, s0, 43
	s_addc_u32 s0, s31, 0
	v_writelane_b32 v254, s0, 42
	s_waitcnt lgkmcnt(0)
	s_barrier
	v_writelane_b32 v254, s92, 45
	s_cmpk_lt_i32 s95, 0x800
	v_writelane_b32 v254, s94, 48
	s_mov_b32 s83, 0
	s_cselect_b64 s[0:1], -1, 0
	s_cmpk_gt_i32 s95, 0x7ff
	s_mul_i32 s35, s94, 0xffffc400
	s_mul_i32 s53, s94, 0x1e00
	v_writelane_b32 v254, s95, 44
	s_cbranch_scc1 .LBB7_447
	v_writelane_b32 v254, s0, 49
	s_and_b32 s87, s95, 15
	s_lshl_b32 s87, s87, 7
	s_lshr_b32 s98, s95, 4
	s_lshl_b32 s98, s98, 3
	s_add_i32 s87, s87, s98
	s_add_i32 s87, s87, s94
	v_writelane_b32 v254, s1, 50
	s_lshl_b32 s0, s94, 14
	s_add_i32 s86, s0, 0
	s_lshl_b32 s88, s3, 3
	s_cmpk_lt_i32 s87, 0x6000
	s_cselect_b64 s[0:1], -1, 0
	v_cndmask_b32_e64 v163, 0, 1, s[0:1]
	s_and_b64 s[0:1], s[0:1], exec
	s_cselect_b32 s2, s87, 0
	s_lshl_b32 s4, s2, 2
	s_and_b32 s33, s4, 0x380
	s_lshl_b32 s4, s2, 5
	s_and_b32 s38, s4, 0x3e0
	s_ashr_i32 s4, s2, 31
	s_lshr_b32 s4, s4, 23
	s_add_i32 s5, s2, s4
	s_ashr_i32 s4, s5, 9
	s_and_b32 s5, s5, 0xfe00
	s_sub_i32 s12, s2, s5
	s_ashr_i32 s5, s4, 31
	s_lshl_b64 s[6:7], s[4:5], 23
	s_lshl_b64 s[10:11], s[4:5], 21
	s_sext_i32_i16 s4, s12
	s_bfe_u32 s4, s4, 0x60019
	s_add_i32 s4, s12, s4
	s_sext_i32_i16 s5, s4
	s_and_b32 s4, s4, 0xffc0
	s_add_i32 s0, s2, 0xffffc000
	s_sub_i32 s4, s12, s4
	s_mov_b32 s9, 0
	s_lshr_b32 s8, s0, 8
	s_lshl_b32 s5, s5, 1
	s_sext_i32_i16 s4, s4
	s_lshl_b64 s[0:1], s[8:9], 20
	s_and_b32 s39, s5, 0xffffff80
	s_lshl_b32 s40, s4, 5
	s_add_i32 s41, s87, s88
	s_cmpk_lt_i32 s41, 0x6000
	s_cselect_b64 s[70:71], -1, 0
	s_lshl_b32 s12, s41, 2
	s_and_b32 s42, s12, 0x380
	s_lshl_b32 s12, s41, 5
	s_and_b32 s43, s12, 0x3e0
	s_ashr_i32 s12, s41, 31
	s_lshr_b32 s12, s12, 23
	s_add_i32 s13, s41, s12
	s_ashr_i32 s12, s13, 9
	s_and_b32 s13, s13, 0xfe00
	s_sub_i32 s34, s41, s13
	s_ashr_i32 s13, s12, 31
	s_lshl_b64 s[16:17], s[12:13], 23
	s_lshl_b64 s[36:37], s[12:13], 21
	s_sext_i32_i16 s12, s34
	s_bfe_u32 s12, s12, 0x60019
	s_add_i32 s12, s34, s12
	s_sext_i32_i16 s13, s12
	s_and_b32 s12, s12, 0xffc0
	s_sub_i32 s12, s34, s12
	s_sext_i32_i16 s12, s12
	s_add_i32 s4, s41, 0xffffc000
	s_lshl_b32 s45, s12, 5
	s_lshl_b32 s12, s94, 8
	s_lshr_b32 s4, s4, 8
	s_mov_b32 s5, s9
	s_lshl_b32 s13, s13, 1
	s_add_i32 s91, s86, s35
	s_add_i32 s97, s12, 0
	s_lshl_b64 s[14:15], s[4:5], 20
	s_and_b32 s44, s13, 0xffffff80
	s_lshl_b32 s89, s3, 4
	s_lshl_b32 s90, s94, 5
	s_lshl_b32 s46, s94, 10
	s_add_i32 s97, s97, 0x1d000
	s_add_i32 s93, s91, s53
	s_lshl_b64 s[12:13], s[8:9], 22
	s_add_u32 s8, s24, s12
	s_addc_u32 s47, s25, s13
	s_add_u32 s48, s20, s6
	s_addc_u32 s49, s21, s7
	s_lshl_b64 s[4:5], s[4:5], 22
	s_add_u32 s50, s24, s4
	s_addc_u32 s51, s25, s5
	v_writelane_b32 v254, s35, 51
	s_add_u32 s52, s20, s16
	v_writelane_b32 v254, s53, 52
	s_addc_u32 s53, s21, s17
	s_add_u32 s68, s30, 0x2000000
	s_addc_u32 s69, s31, 0
	s_add_u32 s84, s30, 0x27000000
	s_addc_u32 s85, s31, 0
	s_add_u32 s34, s30, 0xc000000
	s_addc_u32 s35, s31, 0
	s_add_u32 s6, s30, 0x10000000
	s_addc_u32 s7, s31, 0
	s_add_u32 s92, s30, 0x14000000
	s_addc_u32 s4, s31, 0
	s_cmpk_lt_i32 s2, 0x4000
	s_cselect_b64 s[12:13], -1, 0
	s_mov_b32 s2, 0x27000000
	v_cndmask_b32_e64 v164, 0, 1, s[12:13]
	s_and_b64 s[12:13], s[12:13], exec
	s_cselect_b32 s13, s2, 0x2000000
	s_cselect_b32 s1, s11, s1
	s_cselect_b32 s0, s10, s0
	s_cselect_b32 s5, s39, s33
	s_cselect_b32 s12, s40, s38
	s_cselect_b32 s10, s49, s47
	s_cselect_b32 s8, s48, s8
	s_cselect_b32 s33, 11, 10
	s_add_u32 s11, s30, s13
	s_addc_u32 s13, s31, 0
	s_add_u32 s0, s11, s0
	s_addc_u32 s1, s13, s1
	v_writelane_b32 v254, s0, 53
	s_ashr_i32 s13, s12, 31
	s_waitcnt lgkmcnt(1)
	v_add_f32_e32 v0, v2, v4
	v_writelane_b32 v254, s1, 54
	s_lshl_b64 s[0:1], s[12:13], 2
	s_add_u32 s38, s8, s0
	s_addc_u32 s39, s10, s1
	s_or_b32 s0, s5, 32
	v_writelane_b32 v254, s0, 55
	s_or_b32 s0, s5, 33
	v_writelane_b32 v254, s0, 56
	s_or_b32 s0, s5, 34
	v_writelane_b32 v254, s0, 58
	s_or_b32 s0, s5, 0x41
	v_writelane_b32 v254, s0, 59
	s_or_b32 s0, s5, 0x42
	v_writelane_b32 v254, s0, 61
	s_or_b32 s0, s5, 0x61
	s_or_b32 s82, s5, 64
	s_or_b32 s81, s5, 0x60
	v_writelane_b32 v254, s0, 62
	s_or_b32 s0, s5, 0x62
	s_cmpk_lt_i32 s41, 0x4000
	v_writelane_b32 v254, s0, 63
	s_cselect_b64 s[0:1], -1, 0
	v_cndmask_b32_e64 v165, 0, 1, s[0:1]
	s_and_b64 s[0:1], s[0:1], exec
	s_cselect_b32 s0, s2, 0x2000000
	s_cselect_b32 s1, s37, s15
	s_cselect_b32 s2, s36, s14
	s_cselect_b32 s10, s53, s51
	s_cselect_b32 s11, s52, s50
	s_cselect_b32 s67, s44, s42
	s_cselect_b32 s14, s45, s43
	s_cselect_b32 s52, 11, 10
	s_add_u32 s0, s30, s0
	s_addc_u32 s13, s31, 0
	s_add_u32 s0, s0, s2
	s_waitcnt lgkmcnt(0)
	v_add_f32_e32 v1, v3, v5
	s_addc_u32 s1, s13, s1
	v_mul_f32_e32 v0, 0x3fb8aa3b, v0
	v_mul_f32_e32 v1, 0x3fb8aa3b, v1
	v_writelane_b32 v255, s0, 0
	v_exp_f32_e32 v0, v0
	v_exp_f32_e32 v1, v1
	v_writelane_b32 v255, s1, 1
	s_mov_b32 s0, s14
	s_ashr_i32 s15, s14, 31
	v_writelane_b32 v255, s0, 2
	s_mul_i32 s8, s94, 0xffffe200
	v_sub_f32_e32 v0, v0, v1
	v_writelane_b32 v255, s1, 3
	s_lshl_b64 s[0:1], s[14:15], 2
	s_add_u32 s44, s11, s0
	s_addc_u32 s45, s10, s1
	s_add_i32 s96, s93, s8
	v_add_f32_e32 v162, 0x3e4ccccd, v0
	s_add_i32 s41, s46, 0
	v_mov_b32_e32 v166, 0
	s_mov_b64 s[54:55], 0
	v_mov_b32_e32 v157, 0
	s_mov_b32 s66, 0xc3e00000
	s_movk_i32 s14, 0x7f
	s_add_i32 s15, s91, 0x2000
	s_mov_b64 s[46:47], 0x2000
	s_mov_b64 s[48:49], 0x4000
	s_add_i32 s42, s96, 0xa000
	s_mov_b64 s[50:51], 0x6000
	s_add_i32 s43, s96, 0xe000
	s_movk_i32 s40, 0x110
	v_mov_b32_e32 v167, 0x3727c5ac
	v_mov_b32_e32 v168, 0x43e00000
	v_mov_b32_e32 v178, 0
	v_mov_b32_e32 v177, 0
	v_mov_b32_e32 v176, 0
	v_mov_b32_e32 v175, 0
	v_mov_b32_e32 v174, 0
	v_mov_b32_e32 v173, 0
	v_mov_b32_e32 v172, 0
	v_mov_b32_e32 v161, 0
	v_mov_b32_e32 v160, 0
	v_mov_b32_e32 v155, 0
	v_mov_b32_e32 v154, 0
	v_mov_b32_e32 v153, 0
	v_mov_b32_e32 v152, 0
	v_mov_b32_e32 v151, 0
	v_mov_b32_e32 v150, 0
	v_mov_b32_e32 v145, 0
	s_cmp_lg_u32 s83, s78
	s_cbranch_scc1 .LBB7_433
	s_branch .LBB7_399

; #define LAS __attribute__((address_space(3)))
; __device__ __forceinline__ int fresh_lane() { unsigned z = 0u; asm volatile("" : "+v"(z)); return (int)__builtin_amdgcn_mbcnt_hi(~0u, __builtin_amdgcn_mbcnt_lo(~0u, z)); }
; __device__ __forceinline__ F8Item f8_item(const P& p, int r) {
;     constexpr int I_W1 = 8 * 64, I_W2 = 8 * 32; F8Item it;
;     if (r < NE * I_W1) { const int e = r / I_W1, q = r % I_W1; it.W = p.w1 + (size_t)e * DM * 2048; it.WT = p.ws + WS_W1T + (size_t)e * 2048 * DM; it.N = 2048; it.k0 = 128 * (q / 64); it.n0 = 32 * (q % 64); it.map = 1; }
;     else { r -= NE * I_W1; const int e = r / I_W2, q = r % I_W2; it.W = p.w2 + (size_t)e * DM * DM; it.WT = p.ws + WS_W2T + (size_t)e * DM * DM; it.N = DM; it.k0 = 128 * (q / 32); it.n0 = 32 * (q % 32); it.map = 0; }
;     return it;
; }
; __device__ __forceinline__ void f8_share(const P& p, LAS unsigned char* ring, int G, int vcu, int wave) {
;     const int lane = fresh_lane(); LAS float* scr = (LAS float*)(ring + wave * 16384);
;     const int gw = vcu * NWAVES + wave, NGW = G * NWAVES; constexpr int NF8 = NE * (8 * 64 + 8 * 32);
;     f32x4 va[16], vb[16]; int it = gw;
;     F8Item ia = f8_item(p, it < NF8 ? it : 0), ib = ia;
;     if (it < NF8) f8_load(ia, va, lane);
;     if (it + NGW < NF8) { ib = f8_item(p, it + NGW); f8_load(ib, vb, lane); }
.LBB7_447:
	s_andn2_b64 vcc, exec, s[0:1]
	s_cbranch_vccnz .LBB7_516
	s_lshl_b32 s0, s94, 14
	s_and_b32 s5, s95, 15
	s_lshl_b32 s5, s5, 7
	s_lshr_b32 s98, s95, 4
	s_lshl_b32 s98, s98, 3
	s_add_i32 s5, s5, s98
	s_add_i32 s4, s0, 0
	s_add_i32 s5, s5, s94
	s_lshl_b32 s14, s3, 3
	s_cmpk_lt_i32 s5, 0x6000
	s_cselect_b64 s[0:1], -1, 0
	v_cndmask_b32_e64 v147, 0, 1, s[0:1]
	s_and_b64 s[0:1], s[0:1], exec
	s_cselect_b32 s2, s5, 0
	s_lshl_b32 s8, s2, 2
	s_and_b32 s42, s8, 0x380
	s_lshl_b32 s8, s2, 5
	s_and_b32 s43, s8, 0x3e0
	s_ashr_i32 s8, s2, 31
	s_lshr_b32 s8, s8, 23
	s_add_i32 s9, s2, s8
	s_ashr_i32 s8, s9, 9
	s_and_b32 s9, s9, 0xfe00
	s_sub_i32 s12, s2, s9
	s_sext_i32_i16 s13, s12
	s_bfe_u32 s13, s13, 0x60019
	s_add_i32 s13, s12, s13
	s_sext_i32_i16 s15, s13
	s_and_b32 s13, s13, 0xffc0
	s_add_i32 s0, s2, 0xffffc000
	s_sub_i32 s12, s12, s13
	s_mov_b32 s7, 0
	s_lshr_b32 s6, s0, 8
	s_ashr_i32 s9, s8, 31
	s_lshl_b32 s15, s15, 1
	s_sext_i32_i16 s12, s12
	s_lshl_b64 s[0:1], s[6:7], 20
	s_lshl_b64 s[10:11], s[8:9], 23
	s_lshl_b64 s[8:9], s[8:9], 21
	s_and_b32 s44, s15, 0xffffff80
	s_lshl_b32 s45, s12, 5
	s_add_i32 s46, s5, s14
	s_cmpk_lt_i32 s46, 0x6000
	s_cselect_b64 s[12:13], -1, 0
	s_lshl_b32 s15, s46, 2
	s_and_b32 s47, s15, 0x380
	s_lshl_b32 s15, s46, 5
	s_and_b32 s48, s15, 0x3e0
	s_ashr_i32 s15, s46, 31
	s_lshr_b32 s15, s15, 23
	s_add_i32 s15, s46, s15
	s_ashr_i32 s16, s15, 9
	s_and_b32 s15, s15, 0xfe00
	s_sub_i32 s15, s46, s15
	s_ashr_i32 s17, s16, 31
	s_lshl_b64 s[38:39], s[16:17], 23
	s_lshl_b64 s[40:41], s[16:17], 21
	s_sext_i32_i16 s16, s15
	s_bfe_u32 s16, s16, 0x60019
	s_add_i32 s16, s15, s16
	v_writelane_b32 v254, s5, 55
	s_sext_i32_i16 s17, s16
	s_and_b32 s16, s16, 0xffc0
	v_writelane_b32 v254, s12, 59
	s_sub_i32 s15, s15, s16
	s_lshl_b32 s16, s94, 5
	v_writelane_b32 v254, s13, 60
	s_add_i32 s12, s46, 0xffffc000
	s_and_b32 s34, s16, 0x60
	s_lshl_b32 s16, s94, 8
	s_lshr_b32 s12, s12, 8
	s_mov_b32 s13, s7
	s_lshl_b32 s17, s17, 1
	s_sext_i32_i16 s15, s15
	v_readlane_b32 s58, v254, 4
	s_add_i32 s35, s4, s35
	s_add_i32 s52, s16, 0
	s_lshl_b64 s[36:37], s[12:13], 20
	s_and_b32 s49, s17, 0xffffff80
	s_lshl_b32 s50, s15, 5
	s_lshl_b32 s15, s3, 4
	s_lshr_b32 s33, s58, 8
	s_lshl_b32 s51, s34, 6
	s_lshl_b32 s54, s94, 10
	s_add_i32 s52, s52, 0x1d000
	s_add_i32 s53, s35, s53
	s_lshl_b64 s[16:17], s[6:7], 22
	s_add_u32 s6, s24, s16
	s_addc_u32 s16, s25, s17
	s_add_u32 s17, s20, s10
	s_addc_u32 s55, s21, s11
	s_lshl_b64 s[10:11], s[12:13], 22
	s_add_u32 s56, s24, s10
	s_addc_u32 s57, s25, s11
	s_add_u32 s38, s20, s38
	s_addc_u32 s39, s21, s39
	s_add_u32 s89, s30, 0x2000000
	s_addc_u32 s94, s31, 0
	s_mov_b32 s59, s95
	s_add_u32 s95, s30, 0x27000000
	s_addc_u32 s92, s31, 0
	s_add_u32 s5, s30, 0x6000000
	s_addc_u32 s12, s31, 0
	s_add_u32 s13, s30, 0xa000000
	s_addc_u32 s81, s31, 0
	s_add_u32 s82, s30, 0xb000000
	s_addc_u32 s84, s31, 0
	s_cmpk_lt_i32 s2, 0x4000
	s_cselect_b64 s[10:11], -1, 0
	s_mov_b32 s2, 0x27000000
	v_cndmask_b32_e64 v152, 0, 1, s[10:11]
	s_and_b64 s[10:11], s[10:11], exec
	s_cselect_b32 s11, s2, 0x2000000
	s_cselect_b32 s1, s9, s1
	s_cselect_b32 s0, s8, s0
	s_cselect_b32 s76, s44, s42
	s_cselect_b32 s10, s45, s43
	s_cselect_b32 s8, s55, s16
	s_cselect_b32 s6, s17, s6
	s_cselect_b32 s77, 11, 10
	s_add_u32 s9, s30, s11
	s_addc_u32 s11, s31, 0
	s_add_u32 s0, s9, s0
	s_addc_u32 s1, s11, s1
	v_writelane_b32 v254, s0, 56
	s_ashr_i32 s11, s10, 31
	v_mov_b32_e32 v157, 0
	v_writelane_b32 v254, s1, 57
	s_mov_b32 s0, s10
	v_writelane_b32 v254, s0, 53
	s_mov_b64 s[44:45], 0
	v_mov_b32_e32 v145, 0
	v_writelane_b32 v254, s1, 54
	s_lshl_b64 s[0:1], s[10:11], 2
	s_add_u32 s16, s6, s0
	s_addc_u32 s17, s8, s1
	s_or_b32 s0, s76, 32
	v_writelane_b32 v254, s0, 62
	s_or_b32 s0, s76, 33
	v_writelane_b32 v254, s0, 63
	s_or_b32 s0, s76, 34
	v_writelane_b32 v255, s0, 2
	s_or_b32 s0, s76, 64
	v_writelane_b32 v255, s0, 0
	s_or_b32 s0, s76, 0x41
	v_writelane_b32 v254, s0, 49
	s_or_b32 s0, s76, 0x42
	v_writelane_b32 v254, s0, 51
	s_or_b32 s0, s76, 0x60
	v_writelane_b32 v254, s0, 52
	s_or_b32 s0, s76, 0x61
	v_writelane_b32 v255, s0, 4
	s_or_b32 s0, s76, 0x62
	s_cmpk_lt_i32 s46, 0x4000
	v_writelane_b32 v255, s0, 5
	s_cselect_b64 s[0:1], -1, 0
	v_cndmask_b32_e64 v153, 0, 1, s[0:1]
	s_and_b64 s[0:1], s[0:1], exec
	s_cselect_b32 s0, s2, 0x2000000
	s_cselect_b32 s1, s41, s37
	s_cselect_b32 s2, s40, s36
	s_cselect_b32 s6, s39, s57
	s_cselect_b32 s8, s38, s56
	s_cselect_b32 s9, s49, s47
	s_cselect_b32 s10, s50, s48
	s_cselect_b32 s93, 11, 10
	s_add_u32 s0, s30, s0
	v_writelane_b32 v255, s9, 6
	s_addc_u32 s9, s31, 0
	s_add_u32 s0, s0, s2
	s_addc_u32 s1, s9, s1
	v_writelane_b32 v255, s0, 7
	s_ashr_i32 s11, s10, 31
	s_mov_b32 s41, s59
	v_writelane_b32 v255, s1, 8
	s_mov_b32 s0, s10
	v_writelane_b32 v255, s0, 9
	s_mov_b32 s96, 0xc3e00000
	s_movk_i32 s97, 0x7f
	v_writelane_b32 v255, s1, 10
	s_lshl_b64 s[0:1], s[10:11], 2
	s_add_u32 s42, s8, s0
	s_addc_u32 s43, s6, s1
	s_lshr_b32 s0, s58, 1
	s_and_b32 s0, s0, 0x60
	s_sub_i32 s0, 0, s0
	v_writelane_b32 v254, s0, 58
	s_lshl_b32 s0, s51, 1
	s_add_i32 s39, s54, 0
	s_or_b32 s2, s34, 0xffffff04
	s_add_i32 s10, s35, 0x2000
	s_add_i32 s85, s35, 0x8000
	s_add_i32 s87, s35, 0xa000
	s_add_i32 s88, s35, 0xc000
	s_add_i32 s90, s35, 0xe000
	s_movk_i32 s91, 0xfefe
	v_writelane_b32 v254, s0, 61
	s_movk_i32 s40, 0x110
	v_mov_b32_e32 v154, 0x43e00000
	v_mov_b32_e32 v155, 0xff800000
	v_mov_b32_e32 v156, 0x42800000
	v_mov_b32_e32 v172, 0
	v_mov_b32_e32 v171, 0
	v_mov_b32_e32 v170, 0
	v_mov_b32_e32 v169, 0
	v_mov_b32_e32 v168, 0
	v_mov_b32_e32 v167, 0
	v_mov_b32_e32 v166, 0
	v_mov_b32_e32 v165, 0
	v_mov_b32_e32 v164, 0
	v_mov_b32_e32 v163, 0
	v_mov_b32_e32 v162, 0
	v_mov_b32_e32 v161, 0
	v_mov_b32_e32 v160, 0
	v_mov_b32_e32 v159, 0
	v_mov_b32_e32 v158, 0
	s_cmp_lg_u32 s83, s78
	s_cbranch_scc1 .LBB7_485
	s_branch .LBB7_452
